# speedup vs baseline: 1.0709x; 1.0133x over previous
_Z7k_attn3PKDF16_S0_PKiS2_PiPKDv8_DF16_PKfS6_S8_Pf:
	s_load_dwordx2 s[12:13], s[0:1], 0x8
	s_load_dwordx2 s[4:5], s[0:1], 0x18
	s_load_dwordx2 s[6:7], s[0:1], 0x28
	s_load_dwordx2 s[16:17], s[0:1], 0x10
	v_lshlrev_b32_e32 v13, 4, v0
	s_mul_i32 s3, s2, 0xc350
	v_or_b32_e32 v1, 0x4000, v13
	s_add_i32 s8, s3, 0xc350
	s_lshl_b32 s20, s2, 2
	s_waitcnt lgkmcnt(0)
	s_add_u32 s4, s4, s20
	s_addc_u32 s5, s5, 0
	s_load_dwordx2 s[18:19], s[4:5], 0x0
	global_load_dwordx4 v[100:103], v13, s[6:7]
	global_load_dwordx4 v[104:107], v1, s[6:7]
	v_or_b32_e32 v1, 0x8000, v13
	s_ashr_i32 s9, s8, 31
	v_or_b32_e32 v2, 0xc000, v13
	global_load_dwordx4 v[108:111], v1, s[6:7]
	global_load_dwordx4 v[112:115], v2, s[6:7]
	v_mov_b32_e32 v116, v13
	s_ashr_i32 s6, s3, 31
	s_lshr_b32 s9, s9, 24
	s_lshr_b32 s6, s6, 24
	s_add_i32 s8, s8, s9
	s_add_i32 s3, s3, s6
	v_lshrrev_b32_e32 v80, 6, v0
	s_ashr_i32 s8, s8, 8
	s_ashr_i32 s66, s3, 8
	s_sub_i32 s33, s8, s66
	v_lshlrev_b32_e32 v1, 1, v80
	v_and_b32_e32 v79, 15, v0
	s_add_i32 s67, s33, -1
	v_or_b32_e32 v11, 1, v1
	v_min_i32_e32 v12, s67, v1
	v_min_i32_e32 v10, s67, v11
	v_cmp_gt_u32_e64 s[38:39], 8, v79
	v_bfe_u32 v28, v0, 4, 2
	v_cmp_eq_u32_e32 vcc, 0, v0
	v_cndmask_b32_e64 v1, v10, v12, s[38:39]
	v_add_u32_e32 v2, s66, v1
	v_ashrrev_i32_e32 v3, 31, v2
	v_lshlrev_b64 v[2:3], 8, v[2:3]
	v_and_b32_e32 v1, 0x70, v13
	v_lshl_add_u64 v[8:9], s[12:13], 0, v[2:3]
	v_lshlrev_b32_e32 v2, 1, v1
	v_lshlrev_b32_e32 v1, 3, v28
	v_mov_b32_e32 v3, 0
	v_and_b32_e32 v22, 8, v1
	v_lshl_add_u64 v[8:9], v[8:9], 0, v[2:3]
	v_lshlrev_b32_e32 v26, 1, v22
	v_mov_b32_e32 v27, v3
	v_lshl_add_u64 v[8:9], v[8:9], 0, v[26:27]
	global_load_dwordx4 v[22:25], v[8:9], off nt
	s_and_saveexec_b64 s[6:7], vcc
	v_mov_b32_e32 v3, 16
	v_mov_b32_e32 v4, 0x26b40
	ds_write_b32 v4, v3
	s_or_b64 exec, exec, s[6:7]
	s_movk_i32 s3, 0x100
	v_cmp_gt_u32_e32 vcc, s3, v0
	s_and_saveexec_b64 s[4:5], vcc
	v_mov_b32_e32 v3, 0x1dd00
	v_lshl_add_u32 v3, v0, 2, v3
	v_mov_b32_e32 v4, 0
	ds_write2st64_b32 v3, v4, v4 offset1:4
	s_or_b64 exec, exec, s[4:5]
	s_waitcnt lgkmcnt(0)
	s_cmp_gt_i32 s19, s18
	s_cselect_b64 s[6:7], -1, 0
	s_add_i32 s24, s19, -1
	s_cmp_le_i32 s19, s18
	v_add_u32_e32 v3, s18, v0
	v_mov_b32_e32 v13, 0
	v_mov_b32_e32 v15, 0
	s_barrier
	s_cbranch_scc0 .LBB0_50
	v_cndmask_b32_e64 v4, 0, 1, s[6:7]
	v_cmp_ne_u32_e64 s[4:5], 1, v4
	s_andn2_b64 vcc, exec, s[6:7]
	s_cbranch_vccz .LBB0_51

.LBB0_9:
	v_cmp_gt_i32_e64 s[4:5], s19, v3
	s_waitcnt vmcnt(0)
	ds_write_b128 v116, v[100:103]
	ds_write_b128 v116, v[104:107] offset:16384
	ds_write_b128 v116, v[108:111] offset:32768
	ds_write_b128 v116, v[112:115] offset:49152
	v_ashrrev_i32_e32 v20, 16, v15
	s_and_saveexec_b64 s[6:7], s[4:5]
	v_mov_b32_e32 v4, 0x1dd00
	v_lshl_add_u32 v4, v20, 2, v4
	v_mov_b32_e32 v5, 1
	ds_add_u32 v4, v5
	s_or_b64 exec, exec, s[6:7]
	v_add_u32_e32 v4, 0x400, v3
	v_cmp_gt_i32_e64 s[6:7], s19, v4
	v_ashrrev_i32_e32 v19, 16, v13
	s_and_saveexec_b64 s[8:9], s[6:7]
	v_mov_b32_e32 v4, 0x1dd00
	v_lshl_add_u32 v4, v19, 2, v4
	v_mov_b32_e32 v5, 1
	ds_add_u32 v4, v5
	s_or_b64 exec, exec, s[8:9]
	v_add_u32_e32 v4, 0x800, v3
	v_cmp_gt_i32_e64 s[8:9], s19, v4
	v_ashrrev_i32_e32 v18, 16, v16
	s_and_saveexec_b64 s[10:11], s[8:9]
	v_mov_b32_e32 v4, 0x1dd00
	v_lshl_add_u32 v4, v18, 2, v4
	v_mov_b32_e32 v5, 1
	ds_add_u32 v4, v5
	s_or_b64 exec, exec, s[10:11]
	v_add_u32_e32 v3, 0xc00, v3
	v_cmp_gt_i32_e64 s[10:11], s19, v3
	v_ashrrev_i32_e32 v17, 16, v14
	s_and_saveexec_b64 s[14:15], s[10:11]
	v_mov_b32_e32 v3, 0x1dd00
	v_lshl_add_u32 v3, v17, 2, v3
	v_mov_b32_e32 v4, 1
	ds_add_u32 v3, v4
	s_or_b64 exec, exec, s[14:15]
	s_add_i32 s25, s18, 0x1000
	s_cmp_lt_i32 s25, s19
	s_cselect_b64 s[20:21], -1, 0
	s_cmp_ge_i32 s25, s19
	s_cbranch_scc1 .LBB0_28
	v_mov_b32_e32 v3, 1
	v_mov_b32_e32 v4, 0x1dd00
	s_mov_b32 s3, s25
	s_branch .LBB0_20

.LBB0_97:
	s_or_b64 exec, exec, s[40:41]
	global_load_dword v98, v108, s[58:59]
	global_load_dwordx4 v[74:77], v2, s[92:93]
	global_load_dwordx4 v[94:97], v2, s[92:93] offset:64
	global_load_dwordx4 v[120:123], v2, s[92:93] offset:128
	global_load_dwordx4 v[124:127], v2, s[92:93] offset:192
	s_cmp_lt_i32 s80, 0
	s_cbranch_scc1 .Lattn_skip
	v_mfma_f32_16x16x32_f16 v[104:107], v[66:69], v[6:9], 0
	v_or_b32_e32 v2, s94, v79
	v_cmp_lt_i32_e64 s[42:43], v2, s82
	v_cmp_ge_i32_e64 s[40:41], v2, s82
	v_mfma_f32_16x16x32_f16 v[104:107], v[62:65], v[10:13], v[104:107]
	s_and_b64 s[42:43], s[84:85], s[42:43]
	v_cndmask_b32_e64 v2, 0, 1, s[42:43]
	s_and_b64 s[40:41], s[40:41], s[84:85]
	v_cmp_ne_u32_e64 s[42:43], 0, v2
	v_cndmask_b32_e64 v2, 0, 1, s[40:41]
	v_mfma_f32_16x16x32_f16 v[104:107], v[58:61], v[14:17], v[104:107]
	v_cmp_ne_u32_e32 vcc, 0, v2
	v_mov_b32_e32 v5, s42
	v_cmp_ngt_f32_e64 s[48:49], s70, v103
	v_mov_b32_e32 v2, vcc_lo
	v_cndmask_b32_e64 v2, v2, v5, s[38:39]
	v_mfma_f32_16x16x32_f16 v[108:111], v[54:57], v[18:21], v[104:107]
	v_lshrrev_b32_sdwa v2, v88, v2 dst_sel:DWORD dst_unused:UNUSED_PAD src0_sel:DWORD src1_sel:WORD_0
	v_and_b32_e32 v5, 1, v2
	v_cmp_eq_u32_e64 s[46:47], 0, v5
	v_and_b32_e32 v5, 2, v2
	v_cmp_eq_u32_e64 s[40:41], 0, v5
	v_and_b32_e32 v104, 4, v2
	v_and_b32_e32 v2, 8, v2
	s_nop 0
	v_cndmask_b32_e64 v107, v108, v71, s[46:47]
	v_cndmask_b32_e64 v105, v109, v71, s[40:41]
	v_cmp_eq_u32_e64 s[42:43], 0, v104
	v_cmp_eq_u32_e64 s[44:45], 0, v2
	v_max3_f32 v5, v107, s69, v105
	v_cndmask_b32_e64 v106, v110, v71, s[42:43]
	v_cndmask_b32_e64 v104, v111, v71, s[44:45]
	v_max3_f32 v2, v5, v106, v104
	v_mov_b32_e32 v5, v2
	s_nop 1
	v_permlane16_swap_b32_e32 v5, v2
	v_max_f32_e32 v2, v2, v5
	v_mov_b32_e32 v5, v2
	s_nop 1
	v_permlane32_swap_b32_e32 v5, v2
	v_max_f32_e32 v108, v2, v5
	v_sub_f32_e32 v2, v108, v103
	v_cmp_lt_f32_e32 vcc, s71, v2
	s_and_b64 vcc, s[48:49], vcc
	s_nop 0
	v_cndmask_b32_e64 v2, 0, 1, vcc
	v_cmp_ne_u32_e64 s[50:51], 0, v2
	s_cmp_lg_u64 s[50:51], 0
	s_cselect_b64 s[50:51], -1, 0
	s_cbranch_vccz .LBB0_117
	v_max_f32_e32 v2, v108, v108
	v_max_f32_e32 v5, v103, v103
	v_max_f32_e32 v5, v5, v2
	v_sub_f32_e32 v2, v103, v5
	v_exp_f32_e32 v2, v2
	s_cbranch_execnz .LBB0_100

.Lattn_g_done:
	s_and_saveexec_b64 s[40:41], s[0:1]
	s_cbranch_execz .LBB0_108
	v_mov_b32_e32 v2, v54
	s_waitcnt vmcnt(5)
	v_mov_b32_e32 v99, v112
	v_permlane16_swap_b32_e32 v2, v54
	v_mov_b32_e32 v100, v113
	v_mov_b32_e32 v101, v114
	v_add_f32_e32 v54, v54, v2
	v_mov_b32_e32 v55, v54
	v_mov_b32_e32 v102, v115
	s_nop 0
	v_permlane32_swap_b32_e32 v55, v54
	s_lshl_b32 s95, s80, 1
	v_mov_b32_e32 v2, s95
	v_or_b32_e32 v4, 1, v2
	v_cmp_gt_i32_e32 vcc, s33, v4
	ds_read_b128 v[4:7], v86 offset:32768
	ds_read_b128 v[8:11], v86 offset:33792
	ds_read_b128 v[12:15], v86 offset:34816
	ds_read_b128 v[16:19], v86 offset:35840
	v_cvt_pk_f16_f32 v53, v52, v53
	v_cvt_pk_f16_f32 v52, v50, v51
	v_cvt_pk_f16_f32 v51, v48, v49
	v_cvt_pk_f16_f32 v50, v46, v47
	v_cvt_pk_f16_f32 v45, v44, v45
	v_cvt_pk_f16_f32 v44, v42, v43
	v_cvt_pk_f16_f32 v43, v40, v41
	v_cvt_pk_f16_f32 v42, v38, v39
	v_cvt_pk_f16_f32 v37, v36, v37
	v_cvt_pk_f16_f32 v36, v34, v35
	v_cvt_pk_f16_f32 v35, v32, v33
	v_cvt_pk_f16_f32 v34, v30, v31
	ds_read_b128 v[30:33], v86 offset:36864
	ds_read_b128 v[38:41], v86 offset:37888
	ds_read_b128 v[46:49], v86 offset:38912
	ds_read_b128 v[56:59], v86 offset:39936
	v_cvt_pk_f16_f32 v63, v28, v29
	v_cvt_pk_f16_f32 v62, v26, v27
	v_cvt_pk_f16_f32 v61, v24, v25
	v_cvt_pk_f16_f32 v60, v22, v23
	s_waitcnt lgkmcnt(7)
	v_mfma_f32_16x16x32_f16 v[4:7], v[4:7], v[50:53], 0
	s_waitcnt lgkmcnt(6)
	v_mfma_f32_16x16x32_f16 v[4:7], v[8:11], v[42:45], v[4:7]
	s_waitcnt lgkmcnt(5)
	v_mfma_f32_16x16x32_f16 v[4:7], v[12:15], v[34:37], v[4:7]
	s_waitcnt lgkmcnt(4)
	v_mfma_f32_16x16x32_f16 v[12:15], v[16:19], v[60:63], v[4:7]
	ds_read_b128 v[8:11], v86 offset:44032
	ds_read_b128 v[16:19], v86 offset:43008
	ds_read_b128 v[20:23], v86 offset:41984
	ds_read_b128 v[24:27], v86 offset:40960
	s_waitcnt lgkmcnt(7)
	v_mfma_f32_16x16x32_f16 v[4:7], v[30:33], v[50:53], 0
	s_waitcnt lgkmcnt(6)
	v_mfma_f32_16x16x32_f16 v[4:7], v[38:41], v[42:45], v[4:7]
	s_waitcnt lgkmcnt(5)
	v_mfma_f32_16x16x32_f16 v[4:7], v[46:49], v[34:37], v[4:7]
	s_waitcnt lgkmcnt(4)
	v_mfma_f32_16x16x32_f16 v[4:7], v[56:59], v[60:63], v[4:7]
	ds_read_b128 v[28:31], v86 offset:45056
	ds_read_b128 v[38:41], v86 offset:46080
	ds_read_b128 v[46:49], v86 offset:47104
	ds_read_b128 v[56:59], v86 offset:48128
	s_waitcnt lgkmcnt(4)
	v_mfma_f32_16x16x32_f16 v[24:27], v[24:27], v[50:53], 0
	v_mfma_f32_16x16x32_f16 v[20:23], v[20:23], v[42:45], v[24:27]
	v_mfma_f32_16x16x32_f16 v[16:19], v[16:19], v[34:37], v[20:23]
	v_mfma_f32_16x16x32_f16 v[8:11], v[8:11], v[60:63], v[16:19]
	s_nop 5
	ds_read_b128 v[20:23], v86 offset:52224
	ds_read_b128 v[24:27], v86 offset:51200
	ds_read_b128 v[64:67], v86 offset:50176
	ds_read_b128 v[104:107], v86 offset:49152
	s_waitcnt lgkmcnt(7)
	v_mfma_f32_16x16x32_f16 v[16:19], v[28:31], v[50:53], 0
	s_waitcnt lgkmcnt(6)
	v_mfma_f32_16x16x32_f16 v[16:19], v[38:41], v[42:45], v[16:19]
	s_waitcnt lgkmcnt(5)
	v_mfma_f32_16x16x32_f16 v[16:19], v[46:49], v[34:37], v[16:19]
	s_waitcnt lgkmcnt(4)
	v_mfma_f32_16x16x32_f16 v[16:19], v[56:59], v[60:63], v[16:19]
	ds_read_b128 v[28:31], v86 offset:53248
	ds_read_b128 v[38:41], v86 offset:54272
	ds_read_b128 v[46:49], v86 offset:55296
	ds_read_b128 v[56:59], v86 offset:56320
	s_waitcnt lgkmcnt(4)
	v_mfma_f32_16x16x32_f16 v[104:107], v[104:107], v[50:53], 0
	v_mfma_f32_16x16x32_f16 v[64:67], v[64:67], v[42:45], v[104:107]
	v_mfma_f32_16x16x32_f16 v[24:27], v[24:27], v[34:37], v[64:67]
	v_mfma_f32_16x16x32_f16 v[20:23], v[20:23], v[60:63], v[24:27]
	s_nop 5
	ds_read_b128 v[64:67], v86 offset:60416
	ds_read_b128 v[104:107], v86 offset:59392
	ds_read_b128 v[108:111], v86 offset:58368
	ds_read_b128 v[112:115], v86 offset:57344
	s_waitcnt lgkmcnt(7)
	v_mfma_f32_16x16x32_f16 v[24:27], v[28:31], v[50:53], 0
	s_waitcnt lgkmcnt(6)
	v_mfma_f32_16x16x32_f16 v[24:27], v[38:41], v[42:45], v[24:27]
	s_waitcnt lgkmcnt(5)
	v_mfma_f32_16x16x32_f16 v[24:27], v[46:49], v[34:37], v[24:27]
	s_waitcnt lgkmcnt(4)
	v_mfma_f32_16x16x32_f16 v[24:27], v[56:59], v[60:63], v[24:27]
	ds_read_b128 v[38:41], v86 offset:61440
	ds_read_b128 v[46:49], v86 offset:62464
	ds_read_b128 v[56:59], v86 offset:63488
	ds_read_b128 v[116:119], v86 offset:64512
	s_waitcnt lgkmcnt(4)
	v_mfma_f32_16x16x32_f16 v[28:31], v[112:115], v[50:53], 0
	v_mfma_f32_16x16x32_f16 v[28:31], v[108:111], v[42:45], v[28:31]
	v_mfma_f32_16x16x32_f16 v[28:31], v[104:107], v[34:37], v[28:31]
	v_mfma_f32_16x16x32_f16 v[28:31], v[64:67], v[60:63], v[28:31]
	s_waitcnt lgkmcnt(3)
	v_mfma_f32_16x16x32_f16 v[38:41], v[38:41], v[50:53], 0
	s_waitcnt lgkmcnt(2)
	v_mfma_f32_16x16x32_f16 v[38:41], v[46:49], v[42:45], v[38:41]
	s_waitcnt lgkmcnt(1)
	v_mfma_f32_16x16x32_f16 v[32:35], v[56:59], v[34:37], v[38:41]
	s_waitcnt lgkmcnt(0)
	v_mfma_f32_16x16x32_f16 v[32:35], v[116:119], v[60:63], v[32:35]
	s_or_b64 s[42:43], s[38:39], vcc
	s_and_saveexec_b64 s[0:1], s[42:43]
	s_cbranch_execz .LBB0_105
	v_lshlrev_b32_e32 v36, 1, v78
	ds_read_b128 v[36:39], v36 offset:27472
	v_cndmask_b32_e64 v12, 0, v12, s[14:15]
	v_cndmask_b32_e64 v13, 0, v13, s[14:15]
	v_cndmask_b32_e64 v14, 0, v14, s[14:15]
	v_cndmask_b32_e64 v15, 0, v15, s[14:15]
	v_cndmask_b32_e64 v7, v15, v7, s[12:13]
	v_cndmask_b32_e64 v6, v14, v6, s[12:13]
	v_cndmask_b32_e64 v5, v13, v5, s[12:13]
	v_cndmask_b32_e64 v4, v12, v4, s[12:13]
	v_add_f32_e32 v40, v54, v55
	v_cndmask_b32_e64 v4, v4, v8, s[10:11]
	v_cndmask_b32_e64 v5, v5, v9, s[10:11]
	v_cndmask_b32_e64 v6, v6, v10, s[10:11]
	v_cndmask_b32_e64 v7, v7, v11, s[10:11]
	v_rcp_f32_e32 v12, v40
	v_cndmask_b32_e64 v7, v7, v19, s[8:9]
	v_cndmask_b32_e64 v6, v6, v18, s[8:9]
	v_cndmask_b32_e64 v5, v5, v17, s[8:9]
	v_cndmask_b32_e64 v4, v4, v16, s[8:9]
	v_cndmask_b32_e64 v4, v4, v20, s[6:7]
	v_cndmask_b32_e64 v5, v5, v21, s[6:7]
	v_cndmask_b32_e64 v6, v6, v22, s[6:7]
	v_cndmask_b32_e64 v7, v7, v23, s[6:7]
	v_cndmask_b32_e64 v7, v7, v27, s[20:21]
	v_cndmask_b32_e64 v6, v6, v26, s[20:21]
	v_cndmask_b32_e64 v5, v5, v25, s[20:21]
	v_cndmask_b32_e64 v4, v4, v24, s[20:21]
	v_cmp_lt_f32_e32 vcc, 0, v40
	v_cndmask_b32_e64 v4, v4, v28, s[18:19]
	v_cndmask_b32_e64 v5, v5, v29, s[18:19]
	v_cndmask_b32_e64 v6, v6, v30, s[18:19]
	v_cndmask_b32_e64 v7, v7, v31, s[18:19]
	v_cndmask_b32_e32 v8, 0, v12, vcc
	v_cndmask_b32_e64 v7, v7, v35, s[16:17]
	v_cndmask_b32_e64 v6, v6, v34, s[16:17]
	v_cndmask_b32_e64 v5, v5, v33, s[16:17]
	v_cndmask_b32_e64 v4, v4, v32, s[16:17]
	v_or_b32_e32 v2, v2, v89
	s_waitcnt lgkmcnt(0)
	v_fma_mixlo_f16 v4, v8, v4, v36
	v_fma_mixlo_f16 v5, v8, v5, v37
	v_fma_mixlo_f16 v6, v8, v6, v38
	v_fma_mixlo_f16 v7, v8, v7, v39
	v_cndmask_b32_e32 v4, 0, v4, vcc
	v_cndmask_b32_e32 v8, 0, v5, vcc
	v_cndmask_b32_e32 v5, 0, v6, vcc
	v_cndmask_b32_e32 v6, 0, v7, vcc
	v_pack_b32_f16 v5, v5, v6
	v_pack_b32_f16 v4, v4, v8
	v_mad_u64_u32 v[6:7], s[42:43], v2, s72, v[78:79]
	ds_write_b64 v6, v[4:5]
